# speedup vs baseline: 1.0032x; 1.0032x over previous
.LBB5_223:
	s_or_b64 exec, exec, s[0:1]
	s_movk_i32 s6, 0x290
	v_mad_u32_u24 v26, v77, s6, v74
	s_waitcnt lgkmcnt(0)
	s_barrier
	ds_read_b128 v[28:31], v26
	v_xor_b32_e32 v26, 1, v58
	v_cmp_lt_i32_e32 vcc, v26, v59
	s_mov_b32 s8, 0xf800000
	s_movk_i32 s7, 0x140
	s_waitcnt vmcnt(2) lgkmcnt(0)
	v_pk_add_f32 v[28:29], v[22:23], v[28:29]
	v_pk_add_f32 v[30:31], v[24:25], v[30:31]
	v_add_f32_e32 v22, v28, v29
	v_cndmask_b32_e32 v26, v58, v26, vcc
	v_add_f32_e32 v22, v22, v30
	v_lshlrev_b32_e32 v26, 2, v26
	v_add_f32_e32 v22, v22, v31
	s_nop 1
	v_mov_b32_dpp v24, v22 quad_perm:[1,0,3,2] row_mask:0xf bank_mask:0xf
	v_xor_b32_e32 v23, 2, v58
	v_cmp_lt_i32_e32 vcc, v23, v59
	s_waitcnt lgkmcnt(0)
	v_add_f32_e32 v22, v22, v24
	v_cndmask_b32_e32 v23, v58, v23, vcc
	v_lshlrev_b32_e32 v23, 2, v23
	s_nop 1
	v_mov_b32_dpp v25, v22 quad_perm:[2,3,0,1] row_mask:0xf bank_mask:0xf
	v_xor_b32_e32 v24, 4, v58
	v_cmp_lt_i32_e32 vcc, v24, v59
	s_waitcnt lgkmcnt(0)
	v_add_f32_e32 v22, v22, v25
	v_cndmask_b32_e32 v24, v58, v24, vcc
	v_lshlrev_b32_e32 v24, 2, v24
	s_nop 1
	v_mov_b32_dpp v25, v22 row_half_mirror row_mask:0xf bank_mask:0xf
	s_waitcnt lgkmcnt(0)
	v_add_f32_e32 v22, v22, v25
	s_nop 1
	v_mov_b32_dpp v25, v22 row_mirror row_mask:0xf bank_mask:0xf
	s_waitcnt lgkmcnt(0)
	v_add_f32_e32 v22, v22, v25
	v_mov_b32_e32 v25, v22
	s_nop 1
	v_permlane16_swap_b32_e32 v22, v25
	s_waitcnt lgkmcnt(0)
	v_add_f32_e32 v22, v22, v25
	v_mul_f32_e32 v22, 0x3c000000, v22
	v_pk_add_f32 v[28:29], v[28:29], v[22:23] op_sel_hi:[1,0] neg_lo:[0,1] neg_hi:[0,1]
	v_pk_add_f32 v[30:31], v[30:31], v[22:23] op_sel_hi:[1,0] neg_lo:[0,1] neg_hi:[0,1]
	v_pk_mul_f32 v[32:33], v[28:29], v[28:29]
	v_pk_mul_f32 v[34:35], v[30:31], v[30:31]
	v_add_f32_e32 v22, v32, v33
	v_add_f32_e32 v22, v34, v22
	v_add_f32_e32 v22, v35, v22
	s_nop 1
	v_mov_b32_dpp v25, v22 quad_perm:[1,0,3,2] row_mask:0xf bank_mask:0xf
	v_mov_b64_e32 v[32:33], s[4:5]
	v_mad_i64_i32 v[32:33], s[0:1], v70, s7, v[32:33]
	s_waitcnt lgkmcnt(0)
	v_add_f32_e32 v22, v22, v25
	s_nop 1
	v_mov_b32_dpp v25, v22 quad_perm:[2,3,0,1] row_mask:0xf bank_mask:0xf
	s_waitcnt lgkmcnt(0)
	v_add_f32_e32 v22, v22, v25
	s_nop 1
	v_mov_b32_dpp v25, v22 row_half_mirror row_mask:0xf bank_mask:0xf
	s_waitcnt lgkmcnt(0)
	v_add_f32_e32 v25, v22, v25
	s_nop 1
	v_mov_b32_dpp v27, v25 row_mirror row_mask:0xf bank_mask:0xf
	v_mov_b32_e32 v6, 0x3727c5ac
	v_mov_b32_e32 v22, 0x260
	s_waitcnt lgkmcnt(0)
	v_add_f32_e32 v25, v25, v27
	v_mov_b32_e32 v27, v25
	s_nop 1
	v_permlane16_swap_b32_e32 v25, v27
	v_lshlrev_b32_e32 v0, 1, v1
	v_mov_b32_e32 v1, 0
	v_lshl_add_u64 v[32:33], v[32:33], 0, v[0:1]
	s_waitcnt lgkmcnt(0)
	v_add_f32_e32 v25, v25, v27
	v_fmamk_f32 v25, v25, 0x3c000000, v6
	v_mul_f32_e32 v27, 0x4f800000, v25
	v_cmp_gt_f32_e32 vcc, s8, v25
	s_nop 1
	v_cndmask_b32_e32 v25, v25, v27, vcc
	v_sqrt_f32_e32 v27, v25
	s_nop 0
	v_add_u32_e32 v34, -1, v27
	v_add_u32_e32 v35, 1, v27
	v_fma_f32 v36, -v34, v27, v25
	v_fma_f32 v37, -v35, v27, v25
	v_cmp_ge_f32_e64 s[0:1], 0, v36
	s_nop 1
	v_cndmask_b32_e64 v27, v27, v34, s[0:1]
	v_cmp_lt_f32_e64 s[0:1], 0, v37
	s_nop 1
	v_cndmask_b32_e64 v27, v27, v35, s[0:1]
	v_mul_f32_e32 v34, 0x37800000, v27
	v_cndmask_b32_e32 v27, v27, v34, vcc
	v_cmp_class_f32_e32 vcc, v25, v22
	s_nop 1
	v_cndmask_b32_e32 v25, v27, v25, vcc
	v_div_scale_f32 v27, s[0:1], v25, v25, 1.0
	v_rcp_f32_e32 v34, v27
	v_div_scale_f32 v0, vcc, 1.0, v25, 1.0
	v_fma_f32 v35, -v27, v34, 1.0
	v_fmac_f32_e32 v34, v35, v34
	v_mul_f32_e32 v35, v0, v34
	v_fma_f32 v36, -v27, v35, v0
	v_fmac_f32_e32 v35, v36, v34
	v_fma_f32 v0, -v27, v35, v0
	v_div_fmas_f32 v0, v0, v34, v35
	v_div_fixup_f32 v0, v0, v25, 1.0
	v_pk_mul_f32 v[28:29], v[28:29], v[0:1] op_sel_hi:[1,0]
	v_pk_mul_f32 v[30:31], v[30:31], v[0:1] op_sel_hi:[1,0]
	s_waitcnt vmcnt(0)
	v_pk_fma_f32 v[10:11], v[10:11], v[28:29], v[14:15]
	v_pk_fma_f32 v[12:13], v[12:13], v[30:31], v[16:17]
	v_cvt_pk_f16_f32 v10, v10, v11
	v_cvt_pk_f16_f32 v11, v12, v13
	s_andn2_b64 vcc, exec, s[2:3]
	global_store_dwordx2 v[32:33], v[10:11], off
	s_cbranch_vccnz .LBB5_225
	v_mad_u32_u24 v0, v75, s6, v72
	ds_read_b128 v[10:13], v0 offset:512
	s_waitcnt lgkmcnt(0)
	v_pk_add_f32 v[10:11], v[18:19], v[10:11]
	v_pk_add_f32 v[12:13], v[20:21], v[12:13]
	v_add_f32_e32 v0, v10, v11
	v_add_f32_e32 v0, v0, v12
	v_add_f32_e32 v0, v0, v13
	s_nop 1
	v_mov_b32_dpp v14, v0 quad_perm:[1,0,3,2] row_mask:0xf bank_mask:0xf
	s_waitcnt lgkmcnt(0)
	v_add_f32_e32 v0, v0, v14
	s_nop 1
	v_mov_b32_dpp v14, v0 quad_perm:[2,3,0,1] row_mask:0xf bank_mask:0xf
	s_waitcnt lgkmcnt(0)
	v_add_f32_e32 v0, v0, v14
	s_nop 1
	v_mov_b32_dpp v14, v0 row_half_mirror row_mask:0xf bank_mask:0xf
	s_waitcnt lgkmcnt(0)
	v_add_f32_e32 v0, v0, v14
	v_mul_f32_e32 v0, 0x3d000000, v0
	v_pk_add_f32 v[10:11], v[10:11], v[0:1] op_sel_hi:[1,0] neg_lo:[0,1] neg_hi:[0,1]
	v_pk_add_f32 v[12:13], v[12:13], v[0:1] op_sel_hi:[1,0] neg_lo:[0,1] neg_hi:[0,1]
	v_pk_mul_f32 v[14:15], v[10:11], v[10:11]
	v_pk_mul_f32 v[16:17], v[12:13], v[12:13]
	v_add_f32_e32 v0, v14, v15
	v_add_f32_e32 v0, v16, v0
	v_add_f32_e32 v0, v17, v0
	s_nop 1
	v_mov_b32_dpp v14, v0 quad_perm:[1,0,3,2] row_mask:0xf bank_mask:0xf
	s_waitcnt lgkmcnt(0)
	v_add_f32_e32 v0, v0, v14
	s_nop 1
	v_mov_b32_dpp v14, v0 quad_perm:[2,3,0,1] row_mask:0xf bank_mask:0xf
	s_waitcnt lgkmcnt(0)
	v_add_f32_e32 v0, v0, v14
	s_nop 1
	v_mov_b32_dpp v14, v0 row_half_mirror row_mask:0xf bank_mask:0xf
	s_waitcnt lgkmcnt(0)
	v_add_f32_e32 v0, v0, v14
	v_fmac_f32_e32 v6, 0x3d000000, v0
	v_mul_f32_e32 v0, 0x4f800000, v6
	v_cmp_gt_f32_e32 vcc, s8, v6
	v_mov_b64_e32 v[14:15], s[4:5]
	s_nop 0
	v_cndmask_b32_e32 v16, v6, v0, vcc
	v_sqrt_f32_e32 v17, v16
	v_mov_b32_e32 v6, v67
	v_lshlrev_b32_e32 v0, 1, v71
	v_add_u32_e32 v18, -1, v17
	v_add_u32_e32 v19, 1, v17
	v_fma_f32 v20, -v18, v17, v16
	v_fma_f32 v21, -v19, v17, v16
	v_cmp_ge_f32_e64 s[0:1], 0, v20
	s_nop 1
	v_cndmask_b32_e64 v17, v17, v18, s[0:1]
	v_cmp_lt_f32_e64 s[0:1], 0, v21
	s_nop 1
	v_cndmask_b32_e64 v17, v17, v19, s[0:1]
	v_mul_f32_e32 v18, 0x37800000, v17
	v_cndmask_b32_e32 v17, v17, v18, vcc
	v_cmp_class_f32_e32 vcc, v16, v22
	v_mad_i64_i32 v[14:15], s[0:1], v68, s7, v[14:15]
	s_nop 0
	v_cndmask_b32_e32 v16, v17, v16, vcc
	v_div_scale_f32 v17, s[0:1], v16, v16, 1.0
	v_rcp_f32_e32 v18, v17
	v_div_scale_f32 v19, vcc, 1.0, v16, 1.0
	v_lshl_add_u64 v[0:1], v[14:15], 0, v[0:1]
	v_fma_f32 v20, -v17, v18, 1.0
	v_fmac_f32_e32 v18, v20, v18
	v_mul_f32_e32 v20, v19, v18
	v_fma_f32 v21, -v17, v20, v19
	v_fmac_f32_e32 v20, v21, v18
	v_fma_f32 v17, -v17, v20, v19
	v_div_fmas_f32 v17, v17, v18, v20
	v_div_fixup_f32 v16, v17, v16, 1.0
	v_pk_mul_f32 v[10:11], v[10:11], v[16:17] op_sel_hi:[1,0]
	v_pk_mul_f32 v[12:13], v[12:13], v[16:17] op_sel_hi:[1,0]
	v_pk_fma_f32 v[2:3], v[2:3], v[10:11], v[6:7]
	v_pk_fma_f32 v[4:5], v[4:5], v[12:13], v[8:9]
	v_cvt_pk_f16_f32 v2, v2, v3
	v_cvt_pk_f16_f32 v3, v4, v5
	global_store_dwordx2 v[0:1], v[2:3], off offset:256
